# stats2 hand-written: 48 in-edges cached per node so the serialized >32 loop never runs
# speedup vs baseline: 1.0282x; 1.0045x over previous
_Z13stats2_kernelPKiS0_PKfS2_S0_P15HIP_vector_typeIfLj4EEi:
	s_load_dwordx8 s[4:11], s[0:1], 0x0
	s_load_dwordx4 s[12:15], s[0:1], 0x20
	s_load_dword s16, s[0:1], 0x30
	v_lshrrev_b32_e32 v1, 3, v0
	v_lshl_or_b32 v1, s2, 5, v1
	v_and_b32_e32 v2, 7, v0
	v_mov_b32_e32 v25, 0xff800000
	s_waitcnt lgkmcnt(0)
	s_add_i32 s17, s16, -1
	v_cmp_gt_i32_e64 s[18:19], s16, v1
	v_min_i32_e32 v1, s17, v1
	v_lshlrev_b32_e32 v3, 2, v1
	global_load_dword v4, v3, s[4:5]
	global_load_dword v5, v3, s[4:5] offset:4
	global_load_dword v6, v3, s[10:11]
	global_load_dword v7, v3, s[8:9]
	global_load_dword v8, v3, s[12:13]
	s_waitcnt vmcnt(3)
	v_sub_u32_e32 v5, v5, v4
	v_add_u32_e32 v9, v4, v2
	v_lshlrev_b32_e32 v9, 2, v9
	v_cmp_lt_i32_e64 s[20:21], v2, v5
	v_add_u32_e32 v23, 8, v2
	v_cmp_lt_i32_e64 s[22:23], v23, v5
	v_add_u32_e32 v23, 16, v2
	v_cmp_lt_i32_e64 s[24:25], v23, v5
	v_add_u32_e32 v23, 24, v2
	v_cmp_lt_i32_e64 s[26:27], v23, v5
	v_add_u32_e32 v23, 32, v2
	v_cmp_lt_i32_e64 s[28:29], v23, v5
	v_add_u32_e32 v23, 40, v2
	v_cmp_lt_i32_e64 s[30:31], v23, v5
	s_mov_b64 exec, s[20:21]
	global_load_dword v10, v9, s[6:7]
	s_mov_b64 exec, s[22:23]
	global_load_dword v11, v9, s[6:7] offset:32
	s_mov_b64 exec, s[24:25]
	global_load_dword v12, v9, s[6:7] offset:64
	s_mov_b64 exec, s[26:27]
	global_load_dword v13, v9, s[6:7] offset:96
	s_mov_b64 exec, s[28:29]
	global_load_dword v14, v9, s[6:7] offset:128
	s_mov_b64 exec, s[30:31]
	global_load_dword v15, v9, s[6:7] offset:160
	s_mov_b64 exec, -1
	s_waitcnt vmcnt(0)
	s_mov_b64 exec, s[20:21]
	v_lshlrev_b32_e32 v10, 2, v10
	global_load_dword v10, v10, s[8:9]
	s_mov_b64 exec, s[22:23]
	v_lshlrev_b32_e32 v11, 2, v11
	global_load_dword v11, v11, s[8:9]
	s_mov_b64 exec, s[24:25]
	v_lshlrev_b32_e32 v12, 2, v12
	global_load_dword v12, v12, s[8:9]
	s_mov_b64 exec, s[26:27]
	v_lshlrev_b32_e32 v13, 2, v13
	global_load_dword v13, v13, s[8:9]
	s_mov_b64 exec, s[28:29]
	v_lshlrev_b32_e32 v14, 2, v14
	global_load_dword v14, v14, s[8:9]
	s_mov_b64 exec, s[30:31]
	v_lshlrev_b32_e32 v15, 2, v15
	global_load_dword v15, v15, s[8:9]
	s_mov_b64 exec, -1
	v_add_f32_e32 v22, v6, v7
	v_mul_f32_e32 v23, 0x3e4ccccd, v22
	v_max_f32_e32 v22, v22, v23
	s_waitcnt vmcnt(0)
	v_add_f32_e32 v16, v6, v10
	v_mul_f32_e32 v23, 0x3e4ccccd, v16
	v_max_f32_e32 v16, v16, v23
	v_cndmask_b32_e64 v16, v25, v16, s[20:21]
	v_add_f32_e32 v17, v6, v11
	v_mul_f32_e32 v23, 0x3e4ccccd, v17
	v_max_f32_e32 v17, v17, v23
	v_cndmask_b32_e64 v17, v25, v17, s[22:23]
	v_add_f32_e32 v18, v6, v12
	v_mul_f32_e32 v23, 0x3e4ccccd, v18
	v_max_f32_e32 v18, v18, v23
	v_cndmask_b32_e64 v18, v25, v18, s[24:25]
	v_add_f32_e32 v19, v6, v13
	v_mul_f32_e32 v23, 0x3e4ccccd, v19
	v_max_f32_e32 v19, v19, v23
	v_cndmask_b32_e64 v19, v25, v19, s[26:27]
	v_add_f32_e32 v20, v6, v14
	v_mul_f32_e32 v23, 0x3e4ccccd, v20
	v_max_f32_e32 v20, v20, v23
	v_cndmask_b32_e64 v20, v25, v20, s[28:29]
	v_add_f32_e32 v21, v6, v15
	v_mul_f32_e32 v23, 0x3e4ccccd, v21
	v_max_f32_e32 v21, v21, v23
	v_cndmask_b32_e64 v21, v25, v21, s[30:31]
	v_max3_f32 v24, v22, v16, v17
	v_max3_f32 v24, v24, v18, v19
	v_max3_f32 v24, v24, v20, v21
	v_add_u32_e32 v26, 48, v2
	v_add_u32_e32 v27, 192, v9
.Lst2_mx:
	v_cmp_lt_i32_e32 vcc, v26, v5
	s_and_b64 exec, exec, vcc
	s_cbranch_execz .Lst2_mx_done
	global_load_dword v28, v27, s[6:7]
	s_waitcnt vmcnt(0)
	v_lshlrev_b32_e32 v28, 2, v28
	global_load_dword v28, v28, s[8:9]
	s_waitcnt vmcnt(0)
	v_add_f32_e32 v28, v6, v28
	v_mul_f32_e32 v29, 0x3e4ccccd, v28
	v_max_f32_e32 v28, v28, v29
	v_max_f32_e32 v24, v24, v28
	v_add_u32_e32 v26, 8, v26
	v_add_u32_e32 v27, 32, v27
	s_branch .Lst2_mx
.Lst2_mx_done:
	s_mov_b64 exec, -1
	s_nop 1
	v_mov_b32_dpp v23, v24 quad_perm:[1,0,3,2] row_mask:0xf bank_mask:0xf
	v_max_f32_e32 v24, v24, v23
	s_nop 1
	v_mov_b32_dpp v23, v24 quad_perm:[2,3,0,1] row_mask:0xf bank_mask:0xf
	v_max_f32_e32 v24, v24, v23
	ds_swizzle_b32 v23, v24 offset:swizzle(SWAP,4)
	s_waitcnt lgkmcnt(0)
	v_max_f32_e32 v24, v24, v23
	v_sub_f32_e32 v16, v16, v24
	v_sub_f32_e32 v17, v17, v24
	v_sub_f32_e32 v18, v18, v24
	v_sub_f32_e32 v19, v19, v24
	v_sub_f32_e32 v20, v20, v24
	v_sub_f32_e32 v21, v21, v24
	v_exp_f32_e32 v16, v16
	v_exp_f32_e32 v17, v17
	v_exp_f32_e32 v18, v18
	v_exp_f32_e32 v19, v19
	v_exp_f32_e32 v20, v20
	v_exp_f32_e32 v21, v21
	v_sub_f32_e32 v22, v22, v24
	v_add_f32_e32 v30, v16, v17
	v_add_f32_e32 v31, v18, v19
	v_add_f32_e32 v23, v20, v21
	v_add_f32_e32 v30, v30, v31
	v_add_f32_e32 v30, v30, v23
	v_add_u32_e32 v26, 48, v2
	v_add_u32_e32 v27, 192, v9
.Lst2_sm:
	v_cmp_lt_i32_e32 vcc, v26, v5
	s_and_b64 exec, exec, vcc
	s_cbranch_execz .Lst2_sm_done
	global_load_dword v28, v27, s[6:7]
	s_waitcnt vmcnt(0)
	v_lshlrev_b32_e32 v28, 2, v28
	global_load_dword v28, v28, s[8:9]
	s_waitcnt vmcnt(0)
	v_add_f32_e32 v28, v6, v28
	v_mul_f32_e32 v29, 0x3e4ccccd, v28
	v_max_f32_e32 v28, v28, v29
	v_sub_f32_e32 v28, v28, v24
	v_exp_f32_e32 v28, v28
	s_nop 0
	v_add_f32_e32 v30, v30, v28
	v_add_u32_e32 v26, 8, v26
	v_add_u32_e32 v27, 32, v27
	s_branch .Lst2_sm
.Lst2_sm_done:
	s_mov_b64 exec, -1
	v_exp_f32_e32 v22, v22
	s_nop 1
	v_add_f32_dpp v30, v30, v30 quad_perm:[1,0,3,2] row_mask:0xf bank_mask:0xf
	s_nop 1
	v_add_f32_dpp v30, v30, v30 quad_perm:[2,3,0,1] row_mask:0xf bank_mask:0xf
	ds_swizzle_b32 v23, v30 offset:swizzle(SWAP,4)
	v_cmp_eq_u32_e32 vcc, 0, v2
	s_and_b64 s[18:19], s[18:19], vcc
	s_waitcnt lgkmcnt(0)
	v_add_f32_e32 v30, v30, v23
	v_add_f32_e32 v30, v22, v30
	v_div_scale_f32 v23, s[0:1], v30, v30, 1.0
	v_rcp_f32_e32 v26, v23
	v_div_scale_f32 v27, vcc, 1.0, v30, 1.0
	v_fma_f32 v28, -v23, v26, 1.0
	v_fmac_f32_e32 v26, v28, v26
	v_mul_f32_e32 v28, v27, v26
	v_fma_f32 v29, -v23, v28, v27
	v_fmac_f32_e32 v28, v29, v26
	v_fma_f32 v23, -v23, v28, v27
	v_div_fmas_f32 v23, v23, v26, v28
	v_div_fixup_f32 v14, v23, v30, 1.0
	v_mov_b32_e32 v12, v6
	v_mov_b32_e32 v13, v24
	v_mov_b32_e32 v15, v8
	v_lshlrev_b32_e32 v3, 4, v1
	s_and_saveexec_b64 s[0:1], s[18:19]
	global_store_dwordx4 v3, v[12:15], s[14:15]
	s_endpgm

	.amdhsa_kernel _Z13stats2_kernelPKiS0_PKfS2_S0_P15HIP_vector_typeIfLj4EEi
		.amdhsa_group_segment_fixed_size 0
		.amdhsa_private_segment_fixed_size 0
		.amdhsa_kernarg_size 52
		.amdhsa_user_sgpr_count 2
		.amdhsa_user_sgpr_dispatch_ptr 0
		.amdhsa_user_sgpr_queue_ptr 0
		.amdhsa_user_sgpr_kernarg_segment_ptr 1
		.amdhsa_user_sgpr_dispatch_id 0
		.amdhsa_user_sgpr_kernarg_preload_length 0
		.amdhsa_user_sgpr_kernarg_preload_offset 0
		.amdhsa_user_sgpr_private_segment_size 0
		.amdhsa_uses_dynamic_stack 0
		.amdhsa_enable_private_segment 0
		.amdhsa_system_sgpr_workgroup_id_x 1
		.amdhsa_system_sgpr_workgroup_id_y 0
		.amdhsa_system_sgpr_workgroup_id_z 0
		.amdhsa_system_sgpr_workgroup_info 0
		.amdhsa_system_vgpr_workitem_id 0
		.amdhsa_next_free_vgpr 32
		.amdhsa_next_free_sgpr 32
		.amdhsa_accum_offset 32
		.amdhsa_reserve_vcc 1
		.amdhsa_float_round_mode_32 0
		.amdhsa_float_round_mode_16_64 0
		.amdhsa_float_denorm_mode_32 3
		.amdhsa_float_denorm_mode_16_64 3
		.amdhsa_dx10_clamp 1
		.amdhsa_ieee_mode 1
		.amdhsa_fp16_overflow 0
		.amdhsa_tg_split 0
		.amdhsa_exception_fp_ieee_invalid_op 0
		.amdhsa_exception_fp_denorm_src 0
		.amdhsa_exception_fp_ieee_div_zero 0
		.amdhsa_exception_fp_ieee_overflow 0
		.amdhsa_exception_fp_ieee_underflow 0
		.amdhsa_exception_fp_ieee_inexact 0
		.amdhsa_exception_int_div_zero 0
	.end_amdhsa_kernel

amdhsa.kernels:
  - .agpr_count:     0
    .args:
      - .actual_access:  read_only
        .address_space:  global
        .offset:         0
        .size:           8
        .value_kind:     global_buffer
      - .actual_access:  read_only
        .address_space:  global
        .offset:         8
        .size:           8
        .value_kind:     global_buffer
      - .actual_access:  read_only
        .address_space:  global
        .offset:         16
        .size:           8
        .value_kind:     global_buffer
      - .actual_access:  read_only
        .address_space:  global
        .offset:         24
        .size:           8
        .value_kind:     global_buffer
      - .actual_access:  read_only
        .address_space:  global
        .offset:         32
        .size:           8
        .value_kind:     global_buffer
      - .actual_access:  read_only
        .address_space:  global
        .offset:         40
        .size:           8
        .value_kind:     global_buffer
      - .actual_access:  read_only
        .address_space:  global
        .offset:         48
        .size:           8
        .value_kind:     global_buffer
      - .actual_access:  read_only
        .address_space:  global
        .offset:         56
        .size:           8
        .value_kind:     global_buffer
      - .actual_access:  read_only
        .address_space:  global
        .offset:         64
        .size:           8
        .value_kind:     global_buffer
      - .actual_access:  read_only
        .address_space:  global
        .offset:         72
        .size:           8
        .value_kind:     global_buffer
      - .actual_access:  read_only
        .address_space:  global
        .offset:         80
        .size:           8
        .value_kind:     global_buffer
      - .actual_access:  read_only
        .address_space:  global
        .offset:         88
        .size:           8
        .value_kind:     global_buffer
      - .actual_access:  read_only
        .address_space:  global
        .offset:         96
        .size:           8
        .value_kind:     global_buffer
      - .actual_access:  write_only
        .address_space:  global
        .offset:         104
        .size:           8
        .value_kind:     global_buffer
      - .actual_access:  write_only
        .address_space:  global
        .offset:         112
        .size:           8
        .value_kind:     global_buffer
      - .actual_access:  write_only
        .address_space:  global
        .offset:         120
        .size:           8
        .value_kind:     global_buffer
      - .actual_access:  write_only
        .address_space:  global
        .offset:         128
        .size:           8
        .value_kind:     global_buffer
      - .actual_access:  write_only
        .address_space:  global
        .offset:         136
        .size:           8
        .value_kind:     global_buffer
      - .actual_access:  write_only
        .address_space:  global
        .offset:         144
        .size:           8
        .value_kind:     global_buffer
      - .actual_access:  write_only
        .address_space:  global
        .offset:         152
        .size:           8
        .value_kind:     global_buffer
      - .actual_access:  write_only
        .address_space:  global
        .offset:         160
        .size:           8
        .value_kind:     global_buffer
      - .actual_access:  write_only
        .address_space:  global
        .offset:         168
        .size:           8
        .value_kind:     global_buffer
      - .actual_access:  read_only
        .address_space:  global
        .offset:         176
        .size:           8
        .value_kind:     global_buffer
    .group_segment_fixed_size: 29696
    .kernarg_segment_align: 8
    .kernarg_segment_size: 184
    .language:       OpenCL C
    .language_version:
      - 2
      - 0
    .max_flat_workgroup_size: 512
    .name:           _Z12front_kernelPKiS0_PKfS2_S2_S2_S2_S2_S2_S2_S2_S2_S2_PjS3_PiS4_PDF16_PfS6_S4_S5_S0_
    .private_segment_fixed_size: 0
    .sgpr_count:     30
    .sgpr_spill_count: 0
    .symbol:         _Z12front_kernelPKiS0_PKfS2_S2_S2_S2_S2_S2_S2_S2_S2_S2_PjS3_PiS4_PDF16_PfS6_S4_S5_S0_.kd
    .uniform_work_group_size: 1
    .uses_dynamic_stack: false
    .vgpr_count:     80
    .vgpr_spill_count: 0
    .wavefront_size: 64
  - .agpr_count:     0
    .args:
      - .actual_access:  read_only
        .address_space:  global
        .offset:         0
        .size:           8
        .value_kind:     global_buffer
      - .actual_access:  read_only
        .address_space:  global
        .offset:         8
        .size:           8
        .value_kind:     global_buffer
      - .actual_access:  write_only
        .address_space:  global
        .offset:         16
        .size:           8
        .value_kind:     global_buffer
      - .actual_access:  write_only
        .address_space:  global
        .offset:         24
        .size:           8
        .value_kind:     global_buffer
      - .actual_access:  write_only
        .address_space:  global
        .offset:         32
        .size:           8
        .value_kind:     global_buffer
      - .actual_access:  read_only
        .address_space:  global
        .offset:         40
        .size:           8
        .value_kind:     global_buffer
      - .actual_access:  read_only
        .address_space:  global
        .offset:         48
        .size:           8
        .value_kind:     global_buffer
      - .actual_access:  write_only
        .address_space:  global
        .offset:         56
        .size:           8
        .value_kind:     global_buffer
      - .actual_access:  write_only
        .address_space:  global
        .offset:         64
        .size:           8
        .value_kind:     global_buffer
    .group_segment_fixed_size: 40960
    .kernarg_segment_align: 8
    .kernarg_segment_size: 72
    .language:       OpenCL C
    .language_version:
      - 2
      - 0
    .max_flat_workgroup_size: 512
    .name:           _Z13second_kernelPKfPKDF16_PDF16_PfS4_PKjPKiPiS9_
    .private_segment_fixed_size: 0
    .sgpr_count:     29
    .sgpr_spill_count: 0
    .symbol:         _Z13second_kernelPKfPKDF16_PDF16_PfS4_PKjPKiPiS9_.kd
    .uniform_work_group_size: 1
    .uses_dynamic_stack: false
    .vgpr_count:     64
    .vgpr_spill_count: 0
    .wavefront_size: 64
  - .agpr_count:     0
    .args:
      - .actual_access:  read_only
        .address_space:  global
        .offset:         0
        .size:           8
        .value_kind:     global_buffer
      - .actual_access:  read_only
        .address_space:  global
        .offset:         8
        .size:           8
        .value_kind:     global_buffer
      - .actual_access:  read_only
        .address_space:  global
        .offset:         16
        .size:           8
        .value_kind:     global_buffer
      - .actual_access:  read_only
        .address_space:  global
        .offset:         24
        .size:           8
        .value_kind:     global_buffer
      - .actual_access:  read_only
        .address_space:  global
        .offset:         32
        .size:           8
        .value_kind:     global_buffer
      - .actual_access:  read_only
        .address_space:  global
        .offset:         40
        .size:           8
        .value_kind:     global_buffer
      - .actual_access:  read_only
        .address_space:  global
        .offset:         48
        .size:           8
        .value_kind:     global_buffer
      - .actual_access:  write_only
        .address_space:  global
        .offset:         56
        .size:           8
        .value_kind:     global_buffer
      - .actual_access:  write_only
        .address_space:  global
        .offset:         64
        .size:           8
        .value_kind:     global_buffer
      - .actual_access:  write_only
        .address_space:  global
        .offset:         72
        .size:           8
        .value_kind:     global_buffer
      - .offset:         80
        .size:           4
        .value_kind:     by_value
    .group_segment_fixed_size: 10240
    .kernarg_segment_align: 8
    .kernarg_segment_size: 84
    .language:       OpenCL C
    .language_version:
      - 2
      - 0
    .max_flat_workgroup_size: 256
    .name:           _Z11agg1_kernelPKDF16_PKfS2_PKiS4_S2_S2_PDF16_PfS6_i
    .private_segment_fixed_size: 0
    .sgpr_count:     50
    .sgpr_spill_count: 0
    .symbol:         _Z11agg1_kernelPKDF16_PKfS2_PKiS4_S2_S2_PDF16_PfS6_i.kd
    .uniform_work_group_size: 1
    .uses_dynamic_stack: false
    .vgpr_count:     70
    .vgpr_spill_count: 0
    .wavefront_size: 64
  - .agpr_count:     0
    .args:
      - .actual_access:  read_only
        .address_space:  global
        .offset:         0
        .size:           8
        .value_kind:     global_buffer
      - .actual_access:  read_only
        .address_space:  global
        .offset:         8
        .size:           8
        .value_kind:     global_buffer
      - .actual_access:  read_only
        .address_space:  global
        .offset:         16
        .size:           8
        .value_kind:     global_buffer
      - .actual_access:  read_only
        .address_space:  global
        .offset:         24
        .size:           8
        .value_kind:     global_buffer
      - .actual_access:  read_only
        .address_space:  global
        .offset:         32
        .size:           8
        .value_kind:     global_buffer
      - .actual_access:  write_only
        .address_space:  global
        .offset:         40
        .size:           8
        .value_kind:     global_buffer
      - .offset:         48
        .size:           4
        .value_kind:     by_value
    .group_segment_fixed_size: 0
    .kernarg_segment_align: 8
    .kernarg_segment_size: 52
    .language:       OpenCL C
    .language_version:
      - 2
      - 0
    .max_flat_workgroup_size: 256
    .name:           _Z13stats2_kernelPKiS0_PKfS2_S0_P15HIP_vector_typeIfLj4EEi
    .private_segment_fixed_size: 0
    .sgpr_count:     38
    .sgpr_spill_count: 0
    .symbol:         _Z13stats2_kernelPKiS0_PKfS2_S0_P15HIP_vector_typeIfLj4EEi.kd
    .uniform_work_group_size: 1
    .uses_dynamic_stack: false
    .vgpr_count:     32
    .vgpr_spill_count: 0
    .wavefront_size: 64
  - .agpr_count:     0
    .args:
      - .actual_access:  read_only
        .address_space:  global
        .offset:         0
        .size:           8
        .value_kind:     global_buffer
      - .actual_access:  read_only
        .address_space:  global
        .offset:         8
        .size:           8
        .value_kind:     global_buffer
      - .actual_access:  read_only
        .address_space:  global
        .offset:         16
        .size:           8
        .value_kind:     global_buffer
      - .actual_access:  read_only
        .address_space:  global
        .offset:         24
        .size:           8
        .value_kind:     global_buffer
      - .actual_access:  read_only
        .address_space:  global
        .offset:         32
        .size:           8
        .value_kind:     global_buffer
      - .actual_access:  write_only
        .address_space:  global
        .offset:         40
        .size:           8
        .value_kind:     global_buffer
      - .offset:         48
        .size:           4
        .value_kind:     by_value
    .group_segment_fixed_size: 70752
    .kernarg_segment_align: 8
    .kernarg_segment_size: 52
    .language:       OpenCL C
    .language_version:
      - 2
      - 0
    .max_flat_workgroup_size: 1024
    .name:           _Z12pool2_kernelPKjPKiPKfPK15HIP_vector_typeIfLj4EEPKDF16_Pfi
    .private_segment_fixed_size: 0
    .sgpr_count:     26
    .sgpr_spill_count: 0
    .symbol:         _Z12pool2_kernelPKjPKiPKfPK15HIP_vector_typeIfLj4EEPKDF16_Pfi.kd
    .uniform_work_group_size: 1
    .uses_dynamic_stack: false
    .vgpr_count:     128
    .vgpr_spill_count: 0
    .wavefront_size: 64
  - .agpr_count:     0
    .args:
      - .actual_access:  read_only
        .address_space:  global
        .offset:         0
        .size:           8
        .value_kind:     global_buffer
      - .actual_access:  read_only
        .address_space:  global
        .offset:         8
        .size:           8
        .value_kind:     global_buffer
      - .actual_access:  read_only
        .address_space:  global
        .offset:         16
        .size:           8
        .value_kind:     global_buffer
      - .actual_access:  read_only
        .address_space:  global
        .offset:         24
        .size:           8
        .value_kind:     global_buffer
      - .actual_access:  read_only
        .address_space:  global
        .offset:         32
        .size:           8
        .value_kind:     global_buffer
      - .actual_access:  read_only
        .address_space:  global
        .offset:         40
        .size:           8
        .value_kind:     global_buffer
      - .actual_access:  read_only
        .address_space:  global
        .offset:         48
        .size:           8
        .value_kind:     global_buffer
      - .actual_access:  read_only
        .address_space:  global
        .offset:         56
        .size:           8
        .value_kind:     global_buffer
      - .actual_access:  write_only
        .address_space:  global
        .offset:         64
        .size:           8
        .value_kind:     global_buffer
    .group_segment_fixed_size: 9472
    .kernarg_segment_align: 8
    .kernarg_segment_size: 72
    .language:       OpenCL C
    .language_version:
      - 2
      - 0
    .max_flat_workgroup_size: 1024
    .name:           _Z10mlp_kernelPKfPKiS0_S0_S0_S0_S0_S0_Pf
    .private_segment_fixed_size: 0
    .sgpr_count:     76
    .sgpr_spill_count: 0
    .symbol:         _Z10mlp_kernelPKfPKiS0_S0_S0_S0_S0_S0_Pf.kd
    .uniform_work_group_size: 1
    .uses_dynamic_stack: false
    .vgpr_count:     77
    .vgpr_spill_count: 0
    .wavefront_size: 64
